# speedup vs baseline: 1.0071x; 1.0071x over previous
.Lg1_cloop:
	s_lshl_b32 s12, s8, 14
	v_add3_u32 v42, s12, v37, v35
	v_add3_u32 v58, s12, v36, v35
	s_waitcnt vmcnt(3)
	s_barrier
	ds_read_b128 v[38:41], v42 offset:8192
	ds_read_b128 v[42:45], v42 offset:9216
	ds_read_b128 v[46:49], v58
	ds_read_b128 v[50:53], v58 offset:1024
	ds_read_b128 v[54:57], v58 offset:2048
	ds_read_b128 v[58:61], v58 offset:3072
	s_lshl_b32 s13, s17, 14
	s_add_i32 m0, s13, s16
	s_add_i32 s13, s17, 1
	global_load_lds_dwordx4 v62, s[14:15]
	s_cmp_lg_u32 s17, 4
	s_cselect_b32 s17, s13, 0
	v_add_u32_e32 v62, 64, v62
	s_waitcnt lgkmcnt(0)
	v_mfma_f32_16x16x32_f16 v[30:33], v[46:49], v[38:41], v[30:33]
	s_add_i32 s12, s8, 1
	s_cmp_lg_u32 s8, 4
	s_cselect_b32 s8, s12, 0
	v_mfma_f32_16x16x32_f16 v[22:25], v[46:49], v[42:45], v[22:25]
	s_add_i32 s11, s11, -1
	s_cmp_eq_u32 s11, 0
	v_mfma_f32_16x16x32_f16 v[26:29], v[50:53], v[38:41], v[26:29]
	v_mfma_f32_16x16x32_f16 v[14:17], v[50:53], v[42:45], v[14:17]
	v_mfma_f32_16x16x32_f16 v[18:21], v[54:57], v[38:41], v[18:21]
	v_mfma_f32_16x16x32_f16 v[6:9], v[54:57], v[42:45], v[6:9]
	v_mfma_f32_16x16x32_f16 v[10:13], v[58:61], v[38:41], v[10:13]
	v_mfma_f32_16x16x32_f16 v[2:5], v[58:61], v[42:45], v[2:5]
	s_cbranch_scc0 .Lg1_cloop
	s_or_b32 s8, s10, s4
	v_or_b32_e32 v35, s8, v34
	v_lshl_or_b32 v34, v1, 2, s9
	v_mov_b32_e32 v37, 0
	v_or_b32_e32 v34, s7, v34
	v_lshlrev_b32_e32 v36, 12, v35
	v_mov_b32_e32 v35, v37
	v_lshl_add_u64 v[38:39], s[2:3], 0, v[36:37]
	v_lshlrev_b64 v[40:41], 2, v[34:35]
	v_lshl_add_u64 v[42:43], v[38:39], 0, v[40:41]
	s_mov_b64 s[2:3], 0x10000
	v_lshl_add_u64 v[44:45], v[42:43], 0, s[2:3]
	global_store_dwordx4 v[42:43], v[30:33], off sc1 nt
	global_store_dwordx4 v[42:43], v[26:29], off offset:64 sc1 nt
	global_store_dwordx4 v[42:43], v[18:21], off offset:128 sc1 nt
	global_store_dwordx4 v[42:43], v[10:13], off offset:192 sc1 nt
	global_store_dwordx4 v[44:45], v[22:25], off sc1 nt
	global_store_dwordx4 v[44:45], v[14:17], off offset:64 sc1 nt
	global_store_dwordx4 v[44:45], v[6:9], off offset:128 sc1 nt
	global_store_dwordx4 v[44:45], v[2:5], off offset:192 sc1 nt
	s_branch .LBB3_2
